# E2 conv: 30 conv-weight row loads issued ahead of the glu-staging tail and the stage barrier (on top of the window-fill batching)
# baseline (speedup 1.0000x reference)
; #define LAS __attribute__((address_space(3)))
; __device__ __forceinline__ unsigned pk2(float lo, float hi) { unsigned r; asm("v_cvt_pk_bf16_f32 %0, %1, %2" : "=v"(r) : "v"(lo), "v"(hi)); return r; }
; __device__ __forceinline__ float sigmoidf_(float x) { return __builtin_amdgcn_rcpf(1.0f + __builtin_amdgcn_exp2f(x * -1.44269504089f)); }
; __device__ __forceinline__ void phase_even_mix(CArgs a, LAS unsigned char* lds, int i2, int wv, int xw  ) {
;     ...
;         for (int it = 0; it < 8; ++it) { const int item = it * NTHR + tid, tt = item >> 6, cg = item & 63, p = t0 - 32 + tt;
;             u32x4 o = (u32x4){0u, 0u, 0u, 0u};
;             if (p >= 0) { const bf16* hp = HB + ((size_t)b * SEQ + p) * EVEN_IN + cg * 8; const u32x4 ra = *(const u32x4*)(hp + 512), rg = *(const u32x4*)(hp + 1024);
;                 o.x = pk2(bflo(ra.x) * sigmoidf_(bflo(rg.x)), bfhi(ra.x) * sigmoidf_(bfhi(rg.x))); o.y = pk2(bflo(ra.y) * sigmoidf_(bflo(rg.y)), bfhi(ra.y) * sigmoidf_(bfhi(rg.y)));
;                 o.z = pk2(bflo(ra.z) * sigmoidf_(bflo(rg.z)), bfhi(ra.z) * sigmoidf_(bfhi(rg.z))); o.w = pk2(bflo(ra.w) * sigmoidf_(bflo(rg.w)), bfhi(ra.w) * sigmoidf_(bfhi(rg.w))); }
;             *(LAS u32x4*)(glu + tt * 512 + cg * 8) = o; }
.Le2st_skip7:
	s_or_b64 exec, exec, s[16:17]
	s_waitcnt vmcnt(8)
	v_lshlrev_b32_e32 v1, 16, v232
	v_lshlrev_b32_e32 v10, 16, v236
	v_and_b32_e32 v236, 0xffff0000, v236
	v_lshlrev_b32_e32 v12, 16, v237
	v_and_b32_e32 v237, 0xffff0000, v237
	v_lshlrev_b32_e32 v14, 16, v238
	v_and_b32_e32 v238, 0xffff0000, v238
	v_lshlrev_b32_e32 v16, 16, v239
	v_and_b32_e32 v239, 0xffff0000, v239
	v_mul_f32_e32 v236, 0xbfb8aa3b, v236
	v_mul_f32_e32 v237, 0xbfb8aa3b, v237
	v_mul_f32_e32 v238, 0xbfb8aa3b, v238
	v_mul_f32_e32 v239, 0xbfb8aa3b, v239
	v_mul_f32_e32 v10, 0xbfb8aa3b, v10
	v_mul_f32_e32 v12, 0xbfb8aa3b, v12
	v_mul_f32_e32 v14, 0xbfb8aa3b, v14
	v_mul_f32_e32 v16, 0xbfb8aa3b, v16
	v_exp_f32_e32 v236, v236
	v_exp_f32_e32 v237, v237
	v_exp_f32_e32 v238, v238
	v_exp_f32_e32 v239, v239
	v_exp_f32_e32 v10, v10
	v_exp_f32_e32 v12, v12
	v_exp_f32_e32 v14, v14
	v_exp_f32_e32 v16, v16
	v_add_f32_e32 v236, 1.0, v236
	v_add_f32_e32 v237, 1.0, v237
	v_add_f32_e32 v238, 1.0, v238
	v_add_f32_e32 v239, 1.0, v239
	v_add_f32_e32 v10, 1.0, v10
	v_add_f32_e32 v12, 1.0, v12
	v_add_f32_e32 v14, 1.0, v14
	v_add_f32_e32 v16, 1.0, v16
	v_rcp_f32_e32 v236, v236
	v_rcp_f32_e32 v237, v237
	v_rcp_f32_e32 v238, v238
	v_rcp_f32_e32 v239, v239
	v_rcp_f32_e32 v10, v10
	v_rcp_f32_e32 v12, v12
	v_rcp_f32_e32 v14, v14
	v_rcp_f32_e32 v16, v16
	v_and_b32_e32 v232, 0xffff0000, v232
	v_lshlrev_b32_e32 v11, 16, v233
	v_and_b32_e32 v233, 0xffff0000, v233
	v_lshlrev_b32_e32 v13, 16, v234
	v_and_b32_e32 v234, 0xffff0000, v234
	v_lshlrev_b32_e32 v15, 16, v235
	v_and_b32_e32 v235, 0xffff0000, v235
	v_mul_f32_e32 v232, v236, v232
	v_mul_f32_e32 v233, v237, v233
	v_mul_f32_e32 v234, v238, v234
	v_mul_f32_e32 v235, v239, v235
	v_mul_f32_e32 v1, v10, v1
	v_mul_f32_e32 v236, v12, v11
	v_mul_f32_e32 v237, v14, v13
	v_mul_f32_e32 v238, v16, v15
	v_cvt_pk_bf16_f32 v232, v1, v232
	v_cvt_pk_bf16_f32 v233, v236, v233
	v_cvt_pk_bf16_f32 v234, v237, v234
	v_cvt_pk_bf16_f32 v235, v238, v235
	ds_write_b128 v149, v[232:235]
	s_waitcnt vmcnt(6)
	v_lshlrev_b32_e32 v1, 16, v240
	v_lshlrev_b32_e32 v10, 16, v244
	v_and_b32_e32 v244, 0xffff0000, v244
	v_lshlrev_b32_e32 v12, 16, v245
	v_and_b32_e32 v245, 0xffff0000, v245
	v_lshlrev_b32_e32 v14, 16, v246
	v_and_b32_e32 v246, 0xffff0000, v246
	v_lshlrev_b32_e32 v16, 16, v247
	v_and_b32_e32 v247, 0xffff0000, v247
	v_mul_f32_e32 v244, 0xbfb8aa3b, v244
	v_mul_f32_e32 v245, 0xbfb8aa3b, v245
	v_mul_f32_e32 v246, 0xbfb8aa3b, v246
	v_mul_f32_e32 v247, 0xbfb8aa3b, v247
	v_mul_f32_e32 v10, 0xbfb8aa3b, v10
	v_mul_f32_e32 v12, 0xbfb8aa3b, v12
	v_mul_f32_e32 v14, 0xbfb8aa3b, v14
	v_mul_f32_e32 v16, 0xbfb8aa3b, v16
	v_exp_f32_e32 v244, v244
	v_exp_f32_e32 v245, v245
	v_exp_f32_e32 v246, v246
	v_exp_f32_e32 v247, v247
	v_exp_f32_e32 v10, v10
	v_exp_f32_e32 v12, v12
	v_exp_f32_e32 v14, v14
	v_exp_f32_e32 v16, v16
	v_add_f32_e32 v244, 1.0, v244
	v_add_f32_e32 v245, 1.0, v245
	v_add_f32_e32 v246, 1.0, v246
	v_add_f32_e32 v247, 1.0, v247
	v_add_f32_e32 v10, 1.0, v10
	v_add_f32_e32 v12, 1.0, v12
	v_add_f32_e32 v14, 1.0, v14
	v_add_f32_e32 v16, 1.0, v16
	v_rcp_f32_e32 v244, v244
	v_rcp_f32_e32 v245, v245
	v_rcp_f32_e32 v246, v246
	v_rcp_f32_e32 v247, v247
	v_rcp_f32_e32 v10, v10
	v_rcp_f32_e32 v12, v12
	v_rcp_f32_e32 v14, v14
	v_rcp_f32_e32 v16, v16
	v_and_b32_e32 v240, 0xffff0000, v240
	v_lshlrev_b32_e32 v11, 16, v241
	v_and_b32_e32 v241, 0xffff0000, v241
	v_lshlrev_b32_e32 v13, 16, v242
	v_and_b32_e32 v242, 0xffff0000, v242
	v_lshlrev_b32_e32 v15, 16, v243
	v_and_b32_e32 v243, 0xffff0000, v243
	v_mul_f32_e32 v240, v244, v240
	v_mul_f32_e32 v241, v245, v241
	v_mul_f32_e32 v242, v246, v242
	v_mul_f32_e32 v243, v247, v243
	v_mul_f32_e32 v1, v10, v1
	v_mul_f32_e32 v244, v12, v11
	v_mul_f32_e32 v245, v14, v13
	v_mul_f32_e32 v246, v16, v15
	v_cvt_pk_bf16_f32 v240, v1, v240
	v_cvt_pk_bf16_f32 v241, v244, v241
	v_cvt_pk_bf16_f32 v242, v245, v242
	v_cvt_pk_bf16_f32 v243, v246, v243
	ds_write_b128 v150, v[240:243]
	s_waitcnt vmcnt(4)
	v_lshlrev_b32_e32 v1, 16, v208
	v_lshlrev_b32_e32 v10, 16, v212
	v_and_b32_e32 v212, 0xffff0000, v212
	v_lshlrev_b32_e32 v12, 16, v213
	v_and_b32_e32 v213, 0xffff0000, v213
	v_lshlrev_b32_e32 v14, 16, v214
	v_and_b32_e32 v214, 0xffff0000, v214
	v_lshlrev_b32_e32 v16, 16, v215
	v_and_b32_e32 v215, 0xffff0000, v215
	v_mul_f32_e32 v212, 0xbfb8aa3b, v212
	v_mul_f32_e32 v213, 0xbfb8aa3b, v213
	v_mul_f32_e32 v214, 0xbfb8aa3b, v214
	v_mul_f32_e32 v215, 0xbfb8aa3b, v215
	v_mul_f32_e32 v10, 0xbfb8aa3b, v10
	v_mul_f32_e32 v12, 0xbfb8aa3b, v12
	v_mul_f32_e32 v14, 0xbfb8aa3b, v14
	v_mul_f32_e32 v16, 0xbfb8aa3b, v16
	v_exp_f32_e32 v212, v212
	v_exp_f32_e32 v213, v213
	v_exp_f32_e32 v214, v214
	v_exp_f32_e32 v215, v215
	v_exp_f32_e32 v10, v10
	v_exp_f32_e32 v12, v12
	v_exp_f32_e32 v14, v14
	v_exp_f32_e32 v16, v16
	v_add_f32_e32 v212, 1.0, v212
	v_add_f32_e32 v213, 1.0, v213
	v_add_f32_e32 v214, 1.0, v214
	v_add_f32_e32 v215, 1.0, v215
	v_add_f32_e32 v10, 1.0, v10
	v_add_f32_e32 v12, 1.0, v12
	v_add_f32_e32 v14, 1.0, v14
	v_add_f32_e32 v16, 1.0, v16
	v_rcp_f32_e32 v212, v212
	v_rcp_f32_e32 v213, v213
	v_rcp_f32_e32 v214, v214
	v_rcp_f32_e32 v215, v215
	v_rcp_f32_e32 v10, v10
	v_rcp_f32_e32 v12, v12
	v_rcp_f32_e32 v14, v14
	v_rcp_f32_e32 v16, v16
	v_and_b32_e32 v208, 0xffff0000, v208
	v_lshlrev_b32_e32 v11, 16, v209
	v_and_b32_e32 v209, 0xffff0000, v209
	v_lshlrev_b32_e32 v13, 16, v210
	v_and_b32_e32 v210, 0xffff0000, v210
	v_lshlrev_b32_e32 v15, 16, v211
	v_and_b32_e32 v211, 0xffff0000, v211
	v_mul_f32_e32 v208, v212, v208
	v_mul_f32_e32 v209, v213, v209
	v_mul_f32_e32 v210, v214, v210
	v_mul_f32_e32 v211, v215, v211
	v_mul_f32_e32 v1, v10, v1
	v_mul_f32_e32 v212, v12, v11
	v_mul_f32_e32 v213, v14, v13
	v_mul_f32_e32 v214, v16, v15
	v_cvt_pk_bf16_f32 v208, v1, v208
	v_cvt_pk_bf16_f32 v209, v212, v209
	v_cvt_pk_bf16_f32 v210, v213, v210
	v_cvt_pk_bf16_f32 v211, v214, v211
	ds_write_b128 v151, v[208:211]
	s_waitcnt vmcnt(2)
; #define LAS __attribute__((address_space(3)))
; __device__ __forceinline__ unsigned pk2(float lo, float hi) { unsigned r; asm("v_cvt_pk_bf16_f32 %0, %1, %2" : "=v"(r) : "v"(lo), "v"(hi)); return r; }
; __device__ __forceinline__ float sigmoidf_(float x) { return __builtin_amdgcn_rcpf(1.0f + __builtin_amdgcn_exp2f(x * -1.44269504089f)); }
; __device__ __forceinline__ void phase_even_mix(CArgs a, LAS unsigned char* lds, int i2, int wv, int xw  ) {
;     ...
;         for (int it = 0; it < 8; ++it) { const int item = it * NTHR + tid, tt = item >> 6, cg = item & 63, p = t0 - 32 + tt;
;             u32x4 o = (u32x4){0u, 0u, 0u, 0u};
;             if (p >= 0) { const bf16* hp = HB + ((size_t)b * SEQ + p) * EVEN_IN + cg * 8; const u32x4 ra = *(const u32x4*)(hp + 512), rg = *(const u32x4*)(hp + 1024);
;                 o.x = pk2(bflo(ra.x) * sigmoidf_(bflo(rg.x)), bfhi(ra.x) * sigmoidf_(bfhi(rg.x))); o.y = pk2(bflo(ra.y) * sigmoidf_(bflo(rg.y)), bfhi(ra.y) * sigmoidf_(bfhi(rg.y)));
;                 o.z = pk2(bflo(ra.z) * sigmoidf_(bflo(rg.z)), bfhi(ra.z) * sigmoidf_(bfhi(rg.z))); o.w = pk2(bflo(ra.w) * sigmoidf_(bflo(rg.w)), bfhi(ra.w) * sigmoidf_(bfhi(rg.w))); }
;             *(LAS u32x4*)(glu + tt * 512 + cg * 8) = o; }
;         __syncthreads();
;         {
;             float w[31];
; #pragma unroll
;             for (int k = 0; k < 31; ++k) { unsigned off = (unsigned)c * 4u; asm volatile("" : "+v"(off)); w[k] = *(const float*)((const char*)(cw + k * 512) + off); }
	v_lshlrev_b32_e32 v1, 16, v216
	v_lshlrev_b32_e32 v10, 16, v220
	v_and_b32_e32 v220, 0xffff0000, v220
	v_lshlrev_b32_e32 v12, 16, v221
	v_and_b32_e32 v221, 0xffff0000, v221
	v_lshlrev_b32_e32 v14, 16, v222
	v_and_b32_e32 v222, 0xffff0000, v222
	v_lshlrev_b32_e32 v16, 16, v223
	v_and_b32_e32 v223, 0xffff0000, v223
	v_mul_f32_e32 v220, 0xbfb8aa3b, v220
	v_mul_f32_e32 v221, 0xbfb8aa3b, v221
	v_mul_f32_e32 v222, 0xbfb8aa3b, v222
	v_mul_f32_e32 v223, 0xbfb8aa3b, v223
	v_mul_f32_e32 v10, 0xbfb8aa3b, v10
	v_mul_f32_e32 v12, 0xbfb8aa3b, v12
	v_mul_f32_e32 v14, 0xbfb8aa3b, v14
	v_mul_f32_e32 v16, 0xbfb8aa3b, v16
	v_exp_f32_e32 v220, v220
	v_exp_f32_e32 v221, v221
	v_exp_f32_e32 v222, v222
	v_exp_f32_e32 v223, v223
	v_exp_f32_e32 v10, v10
	v_exp_f32_e32 v12, v12
	v_exp_f32_e32 v14, v14
	v_exp_f32_e32 v16, v16
	v_add_f32_e32 v220, 1.0, v220
	v_add_f32_e32 v221, 1.0, v221
	v_add_f32_e32 v222, 1.0, v222
	v_add_f32_e32 v223, 1.0, v223
	v_add_f32_e32 v10, 1.0, v10
	v_add_f32_e32 v12, 1.0, v12
	v_add_f32_e32 v14, 1.0, v14
	v_add_f32_e32 v16, 1.0, v16
	v_rcp_f32_e32 v220, v220
	v_rcp_f32_e32 v221, v221
	v_rcp_f32_e32 v222, v222
	v_rcp_f32_e32 v223, v223
	v_rcp_f32_e32 v10, v10
	v_rcp_f32_e32 v12, v12
	v_rcp_f32_e32 v14, v14
	v_rcp_f32_e32 v16, v16
	v_and_b32_e32 v216, 0xffff0000, v216
	v_lshlrev_b32_e32 v11, 16, v217
	v_and_b32_e32 v217, 0xffff0000, v217
	v_lshlrev_b32_e32 v13, 16, v218
	v_and_b32_e32 v218, 0xffff0000, v218
	v_lshlrev_b32_e32 v15, 16, v219
	v_and_b32_e32 v219, 0xffff0000, v219
	v_mul_f32_e32 v216, v220, v216
	v_mul_f32_e32 v217, v221, v217
	v_mul_f32_e32 v218, v222, v218
	v_mul_f32_e32 v219, v223, v219
	v_mul_f32_e32 v1, v10, v1
	v_mul_f32_e32 v220, v12, v11
	v_mul_f32_e32 v221, v14, v13
	v_mul_f32_e32 v222, v16, v15
	v_cvt_pk_bf16_f32 v216, v1, v216
	v_cvt_pk_bf16_f32 v217, v220, v217
	v_cvt_pk_bf16_f32 v218, v221, v218
	v_cvt_pk_bf16_f32 v219, v222, v219
	ds_write_b128 v141, v[216:219]
	s_waitcnt vmcnt(0)
	v_mov_b32_e32 v0, v29
	v_mov_b32_e32 v1, v29
	global_load_dword v0, v0, s[90:91]
	v_mov_b32_e32 v2, v29
	v_readlane_b32 s16, v254, 33
	global_load_dword v1, v1, s[90:91] offset:2048
	v_readlane_b32 s17, v254, 34
	v_mov_b32_e32 v3, v29
	v_mov_b32_e32 v4, v29
	v_mov_b32_e32 v5, v29
	v_mov_b32_e32 v6, v29
	v_mov_b32_e32 v7, v29
	global_load_dword v2, v2, s[16:17]
	v_readlane_b32 s16, v254, 35
	v_readlane_b32 s17, v254, 36
	v_mov_b32_e32 v8, v29
	v_mov_b32_e32 v9, v29
	v_mov_b32_e32 v10, v29
	v_mov_b32_e32 v11, v29
	v_mov_b32_e32 v12, v29
	global_load_dword v3, v3, s[16:17]
	v_readlane_b32 s16, v254, 37
	v_readlane_b32 s17, v254, 38
	v_mov_b32_e32 v13, v29
	v_mov_b32_e32 v14, v29
	v_mov_b32_e32 v15, v29
	v_mov_b32_e32 v16, v29
	v_mov_b32_e32 v17, v29
	global_load_dword v4, v4, s[16:17]
	v_readlane_b32 s16, v254, 39
	v_readlane_b32 s17, v254, 40
	v_mov_b32_e32 v18, v29
	v_mov_b32_e32 v19, v29
	v_mov_b32_e32 v20, v29
	v_mov_b32_e32 v21, v29
	v_mov_b32_e32 v22, v29
	global_load_dword v5, v5, s[16:17]
	v_readlane_b32 s16, v254, 41
	v_readlane_b32 s17, v254, 42
	v_mov_b32_e32 v23, v29
	v_mov_b32_e32 v152, v29
	v_mov_b32_e32 v154, v29
	v_mov_b32_e32 v155, v29
	v_mov_b32_e32 v156, v29
	global_load_dword v6, v6, s[16:17]
	v_readlane_b32 s16, v254, 43
	v_readlane_b32 s17, v254, 44
	v_mov_b32_e32 v157, v29
	v_mov_b32_e32 v158, v29
	v_mov_b32_e32 v159, v29
	s_add_i32 s19, s15, -16
	s_nop 0
	global_load_dword v7, v7, s[16:17]
	v_readlane_b32 s16, v254, 45
	v_readlane_b32 s17, v254, 46
	s_nop 4
	global_load_dword v8, v8, s[16:17]
	v_readlane_b32 s16, v254, 47
	v_readlane_b32 s17, v254, 48
	s_nop 4
	global_load_dword v9, v9, s[16:17]
	v_readlane_b32 s16, v254, 49
	v_readlane_b32 s17, v254, 50
	s_nop 4
	global_load_dword v10, v10, s[16:17]
	v_readlane_b32 s16, v254, 51
	v_readlane_b32 s17, v254, 52
	s_nop 4
	global_load_dword v11, v11, s[16:17]
	v_readlane_b32 s16, v254, 53
	v_readlane_b32 s17, v254, 54
	s_nop 4
	global_load_dword v12, v12, s[16:17]
	v_readlane_b32 s16, v254, 55
	v_readlane_b32 s17, v254, 56
	s_nop 4
	global_load_dword v13, v13, s[16:17]
	v_readlane_b32 s16, v254, 57
	v_readlane_b32 s17, v254, 58
	s_nop 4
	global_load_dword v14, v14, s[16:17]
	v_readlane_b32 s16, v254, 59
	v_readlane_b32 s17, v254, 60
	s_nop 4
	global_load_dword v15, v15, s[16:17]
	v_readlane_b32 s16, v254, 61
	v_readlane_b32 s17, v254, 62
	s_nop 4
	global_load_dword v16, v16, s[16:17]
	v_readlane_b32 s16, v254, 63
	v_readlane_b32 s17, v255, 0
	s_nop 4
	global_load_dword v17, v17, s[16:17]
	v_readlane_b32 s16, v255, 1
	v_readlane_b32 s17, v255, 2
	s_nop 4
	global_load_dword v18, v18, s[16:17]
	global_load_dword v19, v19, s[40:41]
	global_load_dword v20, v20, s[84:85]
	global_load_dword v21, v21, s[26:27]
	global_load_dword v22, v22, s[20:21]
	global_load_dword v23, v23, s[4:5]
	global_load_dword v152, v152, s[2:3]
	global_load_dword v154, v154, s[24:25]
	global_load_dword v155, v155, s[30:31]
	global_load_dword v156, v156, s[0:1]
	global_load_dword v157, v157, s[72:73]
	global_load_dword v158, v158, s[74:75]
	v_lshlrev_b32_e32 v63, 16, v224
	v_lshlrev_b32_e32 v64, 16, v228
	v_and_b32_e32 v228, 0xffff0000, v228
	v_lshlrev_b32_e32 v66, 16, v229
	v_and_b32_e32 v229, 0xffff0000, v229
	v_lshlrev_b32_e32 v68, 16, v230
	v_and_b32_e32 v230, 0xffff0000, v230
	v_lshlrev_b32_e32 v179, 16, v231
	v_and_b32_e32 v231, 0xffff0000, v231
	v_mul_f32_e32 v228, 0xbfb8aa3b, v228
	v_mul_f32_e32 v229, 0xbfb8aa3b, v229
	v_mul_f32_e32 v230, 0xbfb8aa3b, v230
	v_mul_f32_e32 v231, 0xbfb8aa3b, v231
	v_mul_f32_e32 v64, 0xbfb8aa3b, v64
	v_mul_f32_e32 v66, 0xbfb8aa3b, v66
	v_mul_f32_e32 v68, 0xbfb8aa3b, v68
	v_mul_f32_e32 v179, 0xbfb8aa3b, v179
	v_exp_f32_e32 v228, v228
	v_exp_f32_e32 v229, v229
	v_exp_f32_e32 v230, v230
	v_exp_f32_e32 v231, v231
	v_exp_f32_e32 v64, v64
	v_exp_f32_e32 v66, v66
	v_exp_f32_e32 v68, v68
	v_exp_f32_e32 v179, v179
	v_add_f32_e32 v228, 1.0, v228
	v_add_f32_e32 v229, 1.0, v229
	v_add_f32_e32 v230, 1.0, v230
	v_add_f32_e32 v231, 1.0, v231
	v_add_f32_e32 v64, 1.0, v64
	v_add_f32_e32 v66, 1.0, v66
	v_add_f32_e32 v68, 1.0, v68
	v_add_f32_e32 v179, 1.0, v179
	v_rcp_f32_e32 v228, v228
	v_rcp_f32_e32 v229, v229
	v_rcp_f32_e32 v230, v230
	v_rcp_f32_e32 v231, v231
	v_rcp_f32_e32 v64, v64
	v_rcp_f32_e32 v66, v66
	v_rcp_f32_e32 v68, v68
	v_rcp_f32_e32 v179, v179
	v_and_b32_e32 v224, 0xffff0000, v224
	v_lshlrev_b32_e32 v65, 16, v225
	v_and_b32_e32 v225, 0xffff0000, v225
	v_lshlrev_b32_e32 v67, 16, v226
	v_and_b32_e32 v226, 0xffff0000, v226
	v_lshlrev_b32_e32 v180, 16, v227
	v_and_b32_e32 v227, 0xffff0000, v227
	v_mul_f32_e32 v224, v228, v224
	v_mul_f32_e32 v225, v229, v225
	v_mul_f32_e32 v226, v230, v226
	v_mul_f32_e32 v227, v231, v227
	v_mul_f32_e32 v63, v64, v63
	v_mul_f32_e32 v228, v66, v65
	v_mul_f32_e32 v229, v68, v67
	v_mul_f32_e32 v230, v179, v180
	v_cvt_pk_bf16_f32 v224, v63, v224
	v_cvt_pk_bf16_f32 v225, v228, v225
	v_cvt_pk_bf16_f32 v226, v229, v226
	v_cvt_pk_bf16_f32 v227, v230, v227
	ds_write_b128 v142, v[224:227]
	s_waitcnt lgkmcnt(0)
	s_barrier
; __device__ __forceinline__ void phase_even_mix(CArgs a, LAS unsigned char* lds, int i2, int wv, int xw  ) {
;     ...
;             const float cb = a->in[I_CONVB][i2 * 512 + c];
;             float win[34];
; #pragma clang loop unroll(full)
;             for (int r = 0; r < 64; ++r) {
;                 win[r % 34] = bf2f(glu[r * 512 + c]);
;                 if (r >= 32) { float y = cb;
; #pragma unroll
;                     for (int k = 0; k < 31; ++k) y += w[k] * win[(r - 30 + k) % 34];
;                     ybuf[(r - 32) * 512 + c] = y; }
	s_load_dwordx2 s[16:17], s[88:89], 0x38
	ds_read_u16 v162, v35 offset:3072
	ds_read_u16 v163, v35 offset:4096
	ds_read_u16 v164, v35 offset:5120
	ds_read_u16 v165, v35 offset:6144
	ds_read_u16 v166, v35 offset:7168
	s_waitcnt lgkmcnt(0)
	v_lshl_add_u64 v[160:161], v[26:27], 2, s[16:17]
	global_load_dword v160, v[160:161], off
	ds_read_u16 v161, v35 offset:2048
	global_load_dword v159, v159, s[76:77]
	v_lshlrev_b32_e32 v167, 16, v166
	ds_read_u16 v174, v35 offset:8192
	ds_read_u16 v176, v35 offset:9216
	ds_read_u16 v177, v35 offset:10240
	ds_read_u16 v192, v35 offset:11264
	ds_read_u16 v193, v35 offset:12288
	ds_read_u16 v194, v35 offset:13312
	ds_read_u16 v196, v35 offset:14336
	ds_read_u16 v198, v35 offset:15360
	ds_read_u16 v205, v35 offset:16384
	ds_read_u16 v204, v35 offset:17408
	ds_read_u16 v203, v35 offset:18432
	ds_read_u16 v202, v35 offset:19456
	ds_read_u16 v201, v35 offset:20480
	s_waitcnt lgkmcnt(0)
	ds_read_u16 v200, v35 offset:21504
	ds_read_u16 v199, v35 offset:22528
	ds_read_u16 v197, v35 offset:23552
	ds_read_u16 v195, v35 offset:24576
	ds_read_u16 v175, v35 offset:25600
	ds_read_u16 v173, v35 offset:26624
	ds_read_u16 v172, v35 offset:27648
	ds_read_u16 v171, v35 offset:28672
	ds_read_u16 v170, v35 offset:29696
	ds_read_u16 v169, v35 offset:30720
	ds_read_u16 v168, v35 offset:31744
	ds_read_u16 v166, v35 offset:32768
	v_lshlrev_b32_e32 v174, 16, v174
	v_lshlrev_b32_e32 v176, 16, v176
	v_lshlrev_b32_e32 v177, 16, v177
	v_lshlrev_b32_e32 v192, 16, v192
	v_lshlrev_b32_e32 v193, 16, v193
	v_lshlrev_b32_e32 v194, 16, v194
	v_lshlrev_b32_e32 v196, 16, v196
	v_lshlrev_b32_e32 v198, 16, v198
	v_lshlrev_b32_e32 v205, 16, v205
	v_lshlrev_b32_e32 v204, 16, v204
	v_lshlrev_b32_e32 v203, 16, v203
	v_lshlrev_b32_e32 v202, 16, v202
	v_lshlrev_b32_e32 v201, 16, v201
	s_waitcnt lgkmcnt(0)
	v_lshlrev_b32_e32 v200, 16, v200
	v_lshlrev_b32_e32 v199, 16, v199
	v_lshlrev_b32_e32 v197, 16, v197
	v_lshlrev_b32_e32 v195, 16, v195
	v_lshlrev_b32_e32 v175, 16, v175
	v_lshlrev_b32_e32 v173, 16, v173
	v_lshlrev_b32_e32 v172, 16, v172
	v_lshlrev_b32_e32 v171, 16, v171
	v_lshlrev_b32_e32 v170, 16, v170
	v_lshlrev_b32_e32 v169, 16, v169
	v_lshlrev_b32_e32 v168, 16, v168
	v_lshlrev_b32_e32 v162, 16, v162
	v_lshlrev_b32_e32 v163, 16, v163
	v_lshlrev_b32_e32 v164, 16, v164
	v_lshlrev_b32_e32 v165, 16, v165
	s_waitcnt vmcnt(1)
	v_fma_f32 v178, v0, v192, v160
	v_fmac_f32_e32 v178, v1, v193
	v_fmac_f32_e32 v178, v2, v194
	v_fmac_f32_e32 v178, v3, v196
	v_fmac_f32_e32 v178, v4, v198
	v_fmac_f32_e32 v178, v5, v205
	v_fmac_f32_e32 v178, v6, v204
	v_fmac_f32_e32 v178, v7, v203
	v_fmac_f32_e32 v178, v8, v202
	v_fmac_f32_e32 v178, v9, v201
	v_fmac_f32_e32 v178, v10, v200
	v_fmac_f32_e32 v178, v11, v199
	v_fmac_f32_e32 v178, v12, v197
	v_fmac_f32_e32 v178, v13, v195
	v_fmac_f32_e32 v178, v14, v175
	v_fmac_f32_e32 v178, v15, v173
	v_fmac_f32_e32 v178, v16, v172
	v_fmac_f32_e32 v178, v17, v171
	v_fmac_f32_e32 v178, v18, v170
	v_fmac_f32_e32 v178, v19, v169
	v_lshlrev_b32_e32 v161, 16, v161
	v_fma_f32 v161, v0, v161, v160
	v_fmac_f32_e32 v161, v1, v162
	v_fmac_f32_e32 v161, v2, v163
	v_fmac_f32_e32 v161, v3, v164
	v_fmac_f32_e32 v161, v4, v165
	v_fmac_f32_e32 v161, v5, v167
	v_fmac_f32_e32 v161, v6, v174
	v_fmac_f32_e32 v161, v7, v176
	v_fma_f32 v162, v0, v162, v160
	v_fmac_f32_e32 v161, v8, v177
	v_fmac_f32_e32 v162, v1, v163
	v_fmac_f32_e32 v161, v9, v192
	v_fmac_f32_e32 v162, v2, v164
	v_fmac_f32_e32 v161, v10, v193
	v_fmac_f32_e32 v162, v3, v165
	v_fmac_f32_e32 v161, v11, v194
	v_fmac_f32_e32 v162, v4, v167
	v_fmac_f32_e32 v161, v12, v196
	v_fmac_f32_e32 v162, v5, v174
	v_fmac_f32_e32 v161, v13, v198
	v_fmac_f32_e32 v162, v6, v176
	v_fmac_f32_e32 v161, v14, v205
	v_fmac_f32_e32 v162, v7, v177
	v_fma_f32 v163, v0, v163, v160
	v_fmac_f32_e32 v161, v15, v204
	v_fmac_f32_e32 v162, v8, v192
	v_fmac_f32_e32 v163, v1, v164
	v_fmac_f32_e32 v161, v16, v203
	v_fmac_f32_e32 v162, v9, v193
	v_fmac_f32_e32 v163, v2, v165
	v_fmac_f32_e32 v161, v17, v202
	v_fmac_f32_e32 v162, v10, v194
	v_fmac_f32_e32 v163, v3, v167
	v_fmac_f32_e32 v161, v18, v201
	v_fmac_f32_e32 v162, v11, v196
	v_fmac_f32_e32 v163, v4, v174
	v_fmac_f32_e32 v161, v19, v200
	v_fmac_f32_e32 v162, v12, v198
	v_fmac_f32_e32 v163, v5, v176
	v_fmac_f32_e32 v161, v20, v199
	v_fmac_f32_e32 v162, v13, v205
	v_fmac_f32_e32 v163, v6, v177
	v_fmac_f32_e32 v161, v21, v197
	v_fmac_f32_e32 v162, v14, v204
	v_fmac_f32_e32 v163, v7, v192
	v_fma_f32 v164, v0, v164, v160
	v_fmac_f32_e32 v161, v22, v195
	v_fmac_f32_e32 v162, v15, v203
	v_fmac_f32_e32 v163, v8, v193
	v_fmac_f32_e32 v164, v1, v165
	v_fmac_f32_e32 v161, v23, v175
	v_fmac_f32_e32 v162, v16, v202
	v_fmac_f32_e32 v163, v9, v194
	v_fmac_f32_e32 v164, v2, v167
	v_fmac_f32_e32 v161, v152, v173
	v_fmac_f32_e32 v162, v17, v201
	v_fmac_f32_e32 v163, v10, v196
	v_fmac_f32_e32 v164, v3, v174
	v_fmac_f32_e32 v161, v154, v172
	v_fmac_f32_e32 v162, v18, v200
	v_fmac_f32_e32 v163, v11, v198
	v_fmac_f32_e32 v164, v4, v176
	v_fmac_f32_e32 v161, v155, v171
	v_fmac_f32_e32 v162, v19, v199
	v_fmac_f32_e32 v163, v12, v205
	v_fmac_f32_e32 v164, v5, v177
	v_fmac_f32_e32 v161, v156, v170
	v_fmac_f32_e32 v162, v20, v197
	v_fmac_f32_e32 v163, v13, v204
	v_fmac_f32_e32 v164, v6, v192
	v_fmac_f32_e32 v161, v157, v169
	v_fmac_f32_e32 v162, v21, v195
	v_fmac_f32_e32 v163, v14, v203
	v_fmac_f32_e32 v164, v7, v193
	v_fma_f32 v165, v0, v165, v160
	s_waitcnt lgkmcnt(0)
	v_lshlrev_b32_e32 v166, 16, v166
	v_fmac_f32_e32 v161, v158, v168
	v_fmac_f32_e32 v162, v22, v175
	v_fmac_f32_e32 v163, v15, v202
	v_fmac_f32_e32 v164, v8, v194
	v_fmac_f32_e32 v165, v1, v167
	s_waitcnt vmcnt(0)
; __device__ __forceinline__ void phase_even_mix(CArgs a, LAS unsigned char* lds, int i2, int wv, int xw  ) {
;     ...
;             for (int r = 0; r < 64; ++r) {
;                 win[r % 34] = bf2f(glu[r * 512 + c]);
;                 if (r >= 32) { float y = cb;
; #pragma unroll
;                     for (int k = 0; k < 31; ++k) y += w[k] * win[(r - 30 + k) % 34];
;                     ybuf[(r - 32) * 512 + c] = y; }
	v_fmac_f32_e32 v161, v159, v166
	v_fmac_f32_e32 v162, v23, v173
	v_fmac_f32_e32 v163, v16, v201
	v_fmac_f32_e32 v164, v9, v196
	v_fmac_f32_e32 v165, v2, v174
	ds_write_b32 v78, v161
	ds_read_u16 v161, v35 offset:33792
	v_fmac_f32_e32 v162, v152, v172
	v_fmac_f32_e32 v163, v17, v200
	v_fmac_f32_e32 v164, v10, v198
	v_fmac_f32_e32 v165, v3, v176
	v_fmac_f32_e32 v162, v154, v171
	v_fmac_f32_e32 v163, v18, v199
	v_fmac_f32_e32 v164, v11, v205
	v_fmac_f32_e32 v165, v4, v177
	v_fmac_f32_e32 v162, v155, v170
	v_fmac_f32_e32 v163, v19, v197
	v_fmac_f32_e32 v164, v12, v204
	v_fmac_f32_e32 v165, v5, v192
	v_fmac_f32_e32 v162, v156, v169
	v_fmac_f32_e32 v163, v20, v195
	v_fmac_f32_e32 v164, v13, v203
	v_fmac_f32_e32 v165, v6, v193
	v_fmac_f32_e32 v162, v157, v168
	v_fmac_f32_e32 v163, v21, v175
	v_fmac_f32_e32 v164, v14, v202
	v_fmac_f32_e32 v165, v7, v194
	v_fma_f32 v167, v0, v167, v160
	s_waitcnt lgkmcnt(0)
	v_lshlrev_b32_e32 v161, 16, v161
	v_fmac_f32_e32 v162, v158, v166
	v_fmac_f32_e32 v163, v22, v173
	v_fmac_f32_e32 v164, v15, v201
	v_fmac_f32_e32 v165, v8, v196
	v_fmac_f32_e32 v167, v1, v174
	v_fmac_f32_e32 v162, v159, v161
	v_fmac_f32_e32 v163, v23, v172
	v_fmac_f32_e32 v164, v16, v200
	v_fmac_f32_e32 v165, v9, v198
	v_fmac_f32_e32 v167, v2, v176
	ds_write_b32 v79, v162
	ds_read_u16 v162, v35 offset:34816
	v_fmac_f32_e32 v163, v152, v171
	v_fmac_f32_e32 v164, v17, v199
	v_fmac_f32_e32 v165, v10, v205
	v_fmac_f32_e32 v167, v3, v177
	v_fmac_f32_e32 v163, v154, v170
	v_fmac_f32_e32 v164, v18, v197
	v_fmac_f32_e32 v165, v11, v204
	v_fmac_f32_e32 v167, v4, v192
	v_fmac_f32_e32 v163, v155, v169
	v_fmac_f32_e32 v164, v19, v195
	v_fmac_f32_e32 v165, v12, v203
	v_fmac_f32_e32 v167, v5, v193
	v_fmac_f32_e32 v163, v156, v168
	v_fmac_f32_e32 v164, v20, v175
	v_fmac_f32_e32 v165, v13, v202
	v_fmac_f32_e32 v167, v6, v194
	v_fmac_f32_e32 v163, v157, v166
	v_fmac_f32_e32 v164, v21, v173
	v_fmac_f32_e32 v165, v14, v201
	v_fmac_f32_e32 v167, v7, v196
	v_fma_f32 v174, v0, v174, v160
	s_waitcnt lgkmcnt(0)
	v_lshlrev_b32_e32 v162, 16, v162
	v_fmac_f32_e32 v163, v158, v161
	v_fmac_f32_e32 v164, v22, v172
	v_fmac_f32_e32 v165, v15, v200
	v_fmac_f32_e32 v167, v8, v198
	v_fmac_f32_e32 v174, v1, v176
	v_fmac_f32_e32 v163, v159, v162
	v_fmac_f32_e32 v164, v23, v171
	v_fmac_f32_e32 v165, v16, v199
	v_fmac_f32_e32 v167, v9, v205
	v_fmac_f32_e32 v174, v2, v177
	ds_write_b32 v80, v163
	ds_read_u16 v163, v35 offset:35840
	v_fmac_f32_e32 v164, v152, v170
	v_fmac_f32_e32 v165, v17, v197
	v_fmac_f32_e32 v167, v10, v204
	v_fmac_f32_e32 v174, v3, v192
	v_fmac_f32_e32 v164, v154, v169
	v_fmac_f32_e32 v165, v18, v195
	v_fmac_f32_e32 v167, v11, v203
	v_fmac_f32_e32 v174, v4, v193
	v_fmac_f32_e32 v164, v155, v168
	v_fmac_f32_e32 v165, v19, v175
	v_fmac_f32_e32 v167, v12, v202
	v_fmac_f32_e32 v174, v5, v194
	v_fmac_f32_e32 v164, v156, v166
	v_fmac_f32_e32 v165, v20, v173
	v_fmac_f32_e32 v167, v13, v201
	v_fmac_f32_e32 v174, v6, v196
	v_fmac_f32_e32 v164, v157, v161
	v_fmac_f32_e32 v165, v21, v172
	v_fmac_f32_e32 v167, v14, v200
	v_fmac_f32_e32 v174, v7, v198
	v_fma_f32 v176, v0, v176, v160
	s_waitcnt lgkmcnt(0)
	v_lshlrev_b32_e32 v163, 16, v163
	v_fmac_f32_e32 v164, v158, v162
	v_fmac_f32_e32 v165, v22, v171
	v_fmac_f32_e32 v167, v15, v199
	v_fmac_f32_e32 v174, v8, v205
	v_fmac_f32_e32 v176, v1, v177
	v_fmac_f32_e32 v164, v159, v163
	v_fmac_f32_e32 v165, v23, v170
	v_fmac_f32_e32 v167, v16, v197
	v_fmac_f32_e32 v174, v9, v204
	v_fmac_f32_e32 v176, v2, v192
	ds_write_b32 v81, v164
	ds_read_u16 v164, v35 offset:36864
	v_fmac_f32_e32 v165, v152, v169
	v_fmac_f32_e32 v167, v17, v195
	v_fmac_f32_e32 v174, v10, v203
	v_fmac_f32_e32 v176, v3, v193
	v_fmac_f32_e32 v165, v154, v168
	v_fmac_f32_e32 v167, v18, v175
	v_fmac_f32_e32 v174, v11, v202
	v_fmac_f32_e32 v176, v4, v194
	v_fmac_f32_e32 v165, v155, v166
	v_fmac_f32_e32 v167, v19, v173
	v_fmac_f32_e32 v174, v12, v201
	v_fmac_f32_e32 v176, v5, v196
	v_fmac_f32_e32 v165, v156, v161
	v_fmac_f32_e32 v167, v20, v172
	v_fmac_f32_e32 v174, v13, v200
	v_fmac_f32_e32 v176, v6, v198
	v_fmac_f32_e32 v165, v157, v162
	v_fmac_f32_e32 v167, v21, v171
	v_fmac_f32_e32 v174, v14, v199
	v_fmac_f32_e32 v176, v7, v205
	v_fma_f32 v177, v0, v177, v160
	s_waitcnt lgkmcnt(0)
	v_lshlrev_b32_e32 v164, 16, v164
	v_fmac_f32_e32 v165, v158, v163
	v_fmac_f32_e32 v167, v22, v170
	v_fmac_f32_e32 v174, v15, v197
	v_fmac_f32_e32 v176, v8, v204
	v_fmac_f32_e32 v177, v1, v192
	v_fmac_f32_e32 v165, v159, v164
	v_fmac_f32_e32 v167, v23, v169
	v_fmac_f32_e32 v174, v16, v195
	v_fmac_f32_e32 v176, v9, v203
	v_fmac_f32_e32 v177, v2, v193
	ds_write_b32 v82, v165
	ds_read_u16 v165, v35 offset:37888
	v_fmac_f32_e32 v167, v152, v168
	v_fmac_f32_e32 v174, v17, v175
	v_fmac_f32_e32 v176, v10, v202
	v_fmac_f32_e32 v177, v3, v194
	v_fmac_f32_e32 v167, v154, v166
	v_fmac_f32_e32 v174, v18, v173
	v_fmac_f32_e32 v176, v11, v201
	v_fmac_f32_e32 v177, v4, v196
	v_fmac_f32_e32 v167, v155, v161
	v_fmac_f32_e32 v174, v19, v172
	v_fmac_f32_e32 v176, v12, v200
	v_fmac_f32_e32 v177, v5, v198
	v_fmac_f32_e32 v167, v156, v162
	v_fmac_f32_e32 v174, v20, v171
	v_fmac_f32_e32 v176, v13, v199
	v_fmac_f32_e32 v177, v6, v205
	v_fmac_f32_e32 v167, v157, v163
	v_fmac_f32_e32 v174, v21, v170
	v_fmac_f32_e32 v176, v14, v197
	v_fmac_f32_e32 v177, v7, v204
	s_waitcnt lgkmcnt(0)
; __device__ __forceinline__ void phase_even_mix(CArgs a, LAS unsigned char* lds, int i2, int wv, int xw  ) {
;     ...
;             for (int r = 0; r < 64; ++r) {
;                 win[r % 34] = bf2f(glu[r * 512 + c]);
;                 if (r >= 32) { float y = cb;
; #pragma unroll
;                     for (int k = 0; k < 31; ++k) y += w[k] * win[(r - 30 + k) % 34];
;                     ybuf[(r - 32) * 512 + c] = y; }
	v_lshlrev_b32_e32 v165, 16, v165
	v_fmac_f32_e32 v167, v158, v164
	v_fmac_f32_e32 v174, v22, v169
	v_fmac_f32_e32 v176, v15, v195
	v_fmac_f32_e32 v177, v8, v203
	v_fmac_f32_e32 v167, v159, v165
	v_fmac_f32_e32 v174, v23, v168
	v_fmac_f32_e32 v176, v16, v175
	v_fmac_f32_e32 v177, v9, v202
	ds_write_b32 v83, v167
	ds_read_u16 v167, v35 offset:38912
	v_fmac_f32_e32 v174, v152, v166
	v_fmac_f32_e32 v176, v17, v173
	v_fmac_f32_e32 v177, v10, v201
	v_fmac_f32_e32 v174, v154, v161
	v_fmac_f32_e32 v176, v18, v172
	v_fmac_f32_e32 v177, v11, v200
	v_fmac_f32_e32 v174, v155, v162
	v_fmac_f32_e32 v176, v19, v171
	v_fmac_f32_e32 v177, v12, v199
	v_fmac_f32_e32 v174, v156, v163
	v_fmac_f32_e32 v176, v20, v170
	v_fmac_f32_e32 v177, v13, v197
	v_fmac_f32_e32 v174, v157, v164
	v_fmac_f32_e32 v176, v21, v169
	v_fmac_f32_e32 v177, v14, v195
	s_waitcnt lgkmcnt(0)
	v_lshlrev_b32_e32 v167, 16, v167
	v_fmac_f32_e32 v174, v158, v165
	v_fmac_f32_e32 v176, v22, v168
	v_fmac_f32_e32 v177, v15, v175
	v_fmac_f32_e32 v174, v159, v167
	v_fmac_f32_e32 v176, v23, v166
	v_fmac_f32_e32 v177, v16, v173
	ds_write_b32 v84, v174
	ds_read_u16 v174, v35 offset:39936
	v_fmac_f32_e32 v176, v152, v161
	v_fmac_f32_e32 v177, v17, v172
	v_fmac_f32_e32 v176, v154, v162
	v_fmac_f32_e32 v177, v18, v171
	v_fmac_f32_e32 v176, v155, v163
	v_fmac_f32_e32 v177, v19, v170
	v_fmac_f32_e32 v176, v156, v164
	v_fmac_f32_e32 v177, v20, v169
	v_fmac_f32_e32 v176, v157, v165
	v_fmac_f32_e32 v177, v21, v168
	s_waitcnt lgkmcnt(0)
	v_lshlrev_b32_e32 v174, 16, v174
	v_fmac_f32_e32 v176, v158, v167
	v_fmac_f32_e32 v177, v22, v166
	v_fmac_f32_e32 v176, v159, v174
	v_fmac_f32_e32 v177, v23, v161
	ds_write_b32 v85, v176
	ds_read_u16 v176, v35 offset:40960
	v_fmac_f32_e32 v177, v152, v162
	v_fmac_f32_e32 v177, v154, v163
	v_fmac_f32_e32 v177, v155, v164
	v_fmac_f32_e32 v177, v156, v165
	v_fmac_f32_e32 v178, v20, v168
	v_fmac_f32_e32 v177, v157, v167
	v_fmac_f32_e32 v178, v21, v166
	s_waitcnt lgkmcnt(0)
	v_lshlrev_b32_e32 v176, 16, v176
	v_fmac_f32_e32 v177, v158, v174
	v_fmac_f32_e32 v178, v22, v161
	v_fmac_f32_e32 v177, v159, v176
	v_fmac_f32_e32 v178, v23, v162
	ds_write_b32 v86, v177
	ds_read_u16 v177, v35 offset:41984
	v_fmac_f32_e32 v178, v152, v163
	v_fmac_f32_e32 v178, v154, v164
	v_fmac_f32_e32 v178, v155, v165
	v_fmac_f32_e32 v178, v156, v167
	v_fmac_f32_e32 v178, v157, v174
	s_waitcnt lgkmcnt(0)
	v_lshlrev_b32_e32 v177, 16, v177
	v_fmac_f32_e32 v178, v158, v176
	v_fmac_f32_e32 v178, v159, v177
	ds_write_b32 v87, v178
	ds_read_u16 v178, v35 offset:43008
	s_waitcnt lgkmcnt(0)
	v_lshlrev_b32_e32 v192, 16, v178
	v_fma_f32 v178, v0, v193, v160
	v_fmac_f32_e32 v178, v1, v194
	v_fmac_f32_e32 v178, v2, v196
	v_fmac_f32_e32 v178, v3, v198
	v_fmac_f32_e32 v178, v4, v205
	v_fmac_f32_e32 v178, v5, v204
	v_fmac_f32_e32 v178, v6, v203
	v_fmac_f32_e32 v178, v7, v202
	v_fmac_f32_e32 v178, v8, v201
	v_fmac_f32_e32 v178, v9, v200
	v_fmac_f32_e32 v178, v10, v199
	v_fmac_f32_e32 v178, v11, v197
	v_fmac_f32_e32 v178, v12, v195
	v_fmac_f32_e32 v178, v13, v175
	v_fmac_f32_e32 v178, v14, v173
	v_fmac_f32_e32 v178, v15, v172
	v_fmac_f32_e32 v178, v16, v171
	v_fmac_f32_e32 v178, v17, v170
	v_fmac_f32_e32 v178, v18, v169
	v_fmac_f32_e32 v178, v19, v168
	v_fmac_f32_e32 v178, v20, v166
	v_fmac_f32_e32 v178, v21, v161
	v_fmac_f32_e32 v178, v22, v162
	v_fmac_f32_e32 v178, v23, v163
	v_fmac_f32_e32 v178, v152, v164
	v_fmac_f32_e32 v178, v154, v165
	v_fmac_f32_e32 v178, v155, v167
	v_fmac_f32_e32 v178, v156, v174
	v_fmac_f32_e32 v178, v157, v176
	v_fmac_f32_e32 v178, v158, v177
	v_fmac_f32_e32 v178, v159, v192
	ds_write_b32 v88, v178
	ds_read_u16 v178, v35 offset:44032
	s_waitcnt lgkmcnt(0)
	v_lshlrev_b32_e32 v193, 16, v178
	v_fma_f32 v178, v0, v194, v160
	v_fmac_f32_e32 v178, v1, v196
	v_fmac_f32_e32 v178, v2, v198
	v_fmac_f32_e32 v178, v3, v205
	v_fmac_f32_e32 v178, v4, v204
	v_fmac_f32_e32 v178, v5, v203
	v_fmac_f32_e32 v178, v6, v202
	v_fmac_f32_e32 v178, v7, v201
	v_fmac_f32_e32 v178, v8, v200
	v_fmac_f32_e32 v178, v9, v199
	v_fmac_f32_e32 v178, v10, v197
	v_fmac_f32_e32 v178, v11, v195
	v_fmac_f32_e32 v178, v12, v175
	v_fmac_f32_e32 v178, v13, v173
	v_fmac_f32_e32 v178, v14, v172
	v_fmac_f32_e32 v178, v15, v171
	v_fmac_f32_e32 v178, v16, v170
	v_fmac_f32_e32 v178, v17, v169
	v_fmac_f32_e32 v178, v18, v168
	v_fmac_f32_e32 v178, v19, v166
	v_fmac_f32_e32 v178, v20, v161
	v_fmac_f32_e32 v178, v21, v162
	v_fmac_f32_e32 v178, v22, v163
	v_fmac_f32_e32 v178, v23, v164
	v_fmac_f32_e32 v178, v152, v165
	v_fmac_f32_e32 v178, v154, v167
	v_fmac_f32_e32 v178, v155, v174
	v_fmac_f32_e32 v178, v156, v176
	v_fmac_f32_e32 v178, v157, v177
	v_fmac_f32_e32 v178, v158, v192
	v_fmac_f32_e32 v178, v159, v193
	ds_write_b32 v89, v178
	ds_read_u16 v178, v35 offset:45056
	s_waitcnt lgkmcnt(0)
	v_lshlrev_b32_e32 v194, 16, v178
	v_fma_f32 v178, v0, v196, v160
	v_fmac_f32_e32 v178, v1, v198
	v_fmac_f32_e32 v178, v2, v205
	v_fmac_f32_e32 v178, v3, v204
	v_fmac_f32_e32 v178, v4, v203
	v_fmac_f32_e32 v178, v5, v202
	v_fmac_f32_e32 v178, v6, v201
	v_fmac_f32_e32 v178, v7, v200
	v_fmac_f32_e32 v178, v8, v199
	v_fmac_f32_e32 v178, v9, v197
	v_fmac_f32_e32 v178, v10, v195
	v_fmac_f32_e32 v178, v11, v175
	v_fmac_f32_e32 v178, v12, v173
	v_fmac_f32_e32 v178, v13, v172
	v_fmac_f32_e32 v178, v14, v171
	v_fmac_f32_e32 v178, v15, v170
	v_fmac_f32_e32 v178, v16, v169
	v_fmac_f32_e32 v178, v17, v168
	v_fmac_f32_e32 v178, v18, v166
	v_fmac_f32_e32 v178, v19, v161
	v_fmac_f32_e32 v178, v20, v162
	v_fmac_f32_e32 v178, v21, v163
	v_fmac_f32_e32 v178, v22, v164
	v_fmac_f32_e32 v178, v23, v165
	v_fmac_f32_e32 v178, v152, v167
	v_fmac_f32_e32 v178, v154, v174
	v_fmac_f32_e32 v178, v155, v176
	v_fmac_f32_e32 v178, v156, v177
	v_fmac_f32_e32 v178, v157, v192
	v_fmac_f32_e32 v178, v158, v193
	v_fmac_f32_e32 v178, v159, v194
	ds_write_b32 v90, v178
	ds_read_u16 v178, v35 offset:46080
	s_waitcnt lgkmcnt(0)
; __device__ __forceinline__ void phase_even_mix(CArgs a, LAS unsigned char* lds, int i2, int wv, int xw  ) {
;     ...
;             for (int r = 0; r < 64; ++r) {
;                 win[r % 34] = bf2f(glu[r * 512 + c]);
;                 if (r >= 32) { float y = cb;
; #pragma unroll
;                     for (int k = 0; k < 31; ++k) y += w[k] * win[(r - 30 + k) % 34];
;                     ybuf[(r - 32) * 512 + c] = y; }
	v_lshlrev_b32_e32 v196, 16, v178
	v_fma_f32 v178, v0, v198, v160
	v_fmac_f32_e32 v178, v1, v205
	v_fmac_f32_e32 v178, v2, v204
	v_fmac_f32_e32 v178, v3, v203
	v_fmac_f32_e32 v178, v4, v202
	v_fmac_f32_e32 v178, v5, v201
	v_fmac_f32_e32 v178, v6, v200
	v_fmac_f32_e32 v178, v7, v199
	v_fmac_f32_e32 v178, v8, v197
	v_fmac_f32_e32 v178, v9, v195
	v_fmac_f32_e32 v178, v10, v175
	v_fmac_f32_e32 v178, v11, v173
	v_fmac_f32_e32 v178, v12, v172
	v_fmac_f32_e32 v178, v13, v171
	v_fmac_f32_e32 v178, v14, v170
	v_fmac_f32_e32 v178, v15, v169
	v_fmac_f32_e32 v178, v16, v168
	v_fmac_f32_e32 v178, v17, v166
	v_fmac_f32_e32 v178, v18, v161
	v_fmac_f32_e32 v178, v19, v162
	v_fmac_f32_e32 v178, v20, v163
	v_fmac_f32_e32 v178, v21, v164
	v_fmac_f32_e32 v178, v22, v165
	v_fmac_f32_e32 v178, v23, v167
	v_fmac_f32_e32 v178, v152, v174
	v_fmac_f32_e32 v178, v154, v176
	v_fmac_f32_e32 v178, v155, v177
	v_fmac_f32_e32 v178, v156, v192
	v_fmac_f32_e32 v178, v157, v193
	v_fmac_f32_e32 v178, v158, v194
	v_fmac_f32_e32 v178, v159, v196
	ds_write_b32 v91, v178
	ds_read_u16 v178, v35 offset:47104
	s_waitcnt lgkmcnt(0)
	v_lshlrev_b32_e32 v198, 16, v178
	v_fma_f32 v178, v0, v205, v160
	v_fmac_f32_e32 v178, v1, v204
	v_fmac_f32_e32 v178, v2, v203
	v_fmac_f32_e32 v178, v3, v202
	v_fmac_f32_e32 v178, v4, v201
	v_fmac_f32_e32 v178, v5, v200
	v_fmac_f32_e32 v178, v6, v199
	v_fmac_f32_e32 v178, v7, v197
	v_fmac_f32_e32 v178, v8, v195
	v_fmac_f32_e32 v178, v9, v175
	v_fmac_f32_e32 v178, v10, v173
	v_fmac_f32_e32 v178, v11, v172
	v_fmac_f32_e32 v178, v12, v171
	v_fmac_f32_e32 v178, v13, v170
	v_fmac_f32_e32 v178, v14, v169
	v_fmac_f32_e32 v178, v15, v168
	v_fmac_f32_e32 v178, v16, v166
	v_fmac_f32_e32 v178, v17, v161
	v_fmac_f32_e32 v178, v18, v162
	v_fmac_f32_e32 v178, v19, v163
	v_fmac_f32_e32 v178, v20, v164
	v_fmac_f32_e32 v178, v21, v165
	v_fmac_f32_e32 v178, v22, v167
	v_fmac_f32_e32 v178, v23, v174
	v_fmac_f32_e32 v178, v152, v176
	v_fmac_f32_e32 v178, v154, v177
	v_fmac_f32_e32 v178, v155, v192
	v_fmac_f32_e32 v178, v156, v193
	v_fmac_f32_e32 v178, v157, v194
	v_fmac_f32_e32 v178, v158, v196
	v_fmac_f32_e32 v178, v159, v198
	ds_write_b32 v92, v178
	v_fma_f32 v178, v0, v204, v160
	v_fmac_f32_e32 v178, v1, v203
	v_fmac_f32_e32 v178, v2, v202
	v_fmac_f32_e32 v178, v3, v201
	v_fmac_f32_e32 v178, v4, v200
	v_fmac_f32_e32 v178, v5, v199
	v_fmac_f32_e32 v178, v6, v197
	v_fmac_f32_e32 v178, v7, v195
	v_fmac_f32_e32 v178, v8, v175
	v_fmac_f32_e32 v178, v9, v173
	v_fmac_f32_e32 v178, v10, v172
	v_fmac_f32_e32 v178, v11, v171
	v_fmac_f32_e32 v178, v12, v170
	v_fmac_f32_e32 v178, v13, v169
	v_fmac_f32_e32 v178, v14, v168
	v_fmac_f32_e32 v178, v15, v166
	v_fmac_f32_e32 v178, v16, v161
	v_fmac_f32_e32 v178, v17, v162
	v_fmac_f32_e32 v178, v18, v163
	v_fmac_f32_e32 v178, v19, v164
	v_fmac_f32_e32 v178, v20, v165
	v_fmac_f32_e32 v178, v21, v167
	v_fmac_f32_e32 v178, v22, v174
	v_fmac_f32_e32 v178, v23, v176
	ds_read_u16 v205, v35 offset:48128
	v_fmac_f32_e32 v178, v152, v177
	v_fmac_f32_e32 v178, v154, v192
	v_fmac_f32_e32 v178, v155, v193
	v_fmac_f32_e32 v178, v156, v194
	v_fmac_f32_e32 v178, v157, v196
	s_waitcnt lgkmcnt(0)
	v_lshlrev_b32_e32 v205, 16, v205
	v_fmac_f32_e32 v178, v158, v198
	v_fmac_f32_e32 v178, v159, v205
	ds_write_b32 v93, v178
	ds_read_u16 v178, v35 offset:49152
	s_waitcnt lgkmcnt(0)
	v_lshlrev_b32_e32 v204, 16, v178
	v_fma_f32 v178, v0, v203, v160
	v_fmac_f32_e32 v178, v1, v202
	v_fmac_f32_e32 v178, v2, v201
	v_fmac_f32_e32 v178, v3, v200
	v_fmac_f32_e32 v178, v4, v199
	v_fmac_f32_e32 v178, v5, v197
	v_fmac_f32_e32 v178, v6, v195
	v_fmac_f32_e32 v178, v7, v175
	v_fmac_f32_e32 v178, v8, v173
	v_fmac_f32_e32 v178, v9, v172
	v_fmac_f32_e32 v178, v10, v171
	v_fmac_f32_e32 v178, v11, v170
	v_fmac_f32_e32 v178, v12, v169
	v_fmac_f32_e32 v178, v13, v168
	v_fmac_f32_e32 v178, v14, v166
	v_fmac_f32_e32 v178, v15, v161
	v_fmac_f32_e32 v178, v16, v162
	v_fmac_f32_e32 v178, v17, v163
	v_fmac_f32_e32 v178, v18, v164
	v_fmac_f32_e32 v178, v19, v165
	v_fmac_f32_e32 v178, v20, v167
	v_fmac_f32_e32 v178, v21, v174
	v_fmac_f32_e32 v178, v22, v176
	v_fmac_f32_e32 v178, v23, v177
	v_fmac_f32_e32 v178, v152, v192
	v_fmac_f32_e32 v178, v154, v193
	v_fmac_f32_e32 v178, v155, v194
	v_fmac_f32_e32 v178, v156, v196
	v_fmac_f32_e32 v178, v157, v198
	v_fmac_f32_e32 v178, v158, v205
	v_fmac_f32_e32 v178, v159, v204
	ds_write_b32 v94, v178
	ds_read_u16 v178, v35 offset:50176
	s_waitcnt lgkmcnt(0)
	v_lshlrev_b32_e32 v203, 16, v178
	v_fma_f32 v178, v0, v202, v160
	v_fmac_f32_e32 v178, v1, v201
	v_fmac_f32_e32 v178, v2, v200
	v_fmac_f32_e32 v178, v3, v199
	v_fmac_f32_e32 v178, v4, v197
	v_fmac_f32_e32 v178, v5, v195
	v_fmac_f32_e32 v178, v6, v175
	v_fmac_f32_e32 v178, v7, v173
	v_fmac_f32_e32 v178, v8, v172
	v_fmac_f32_e32 v178, v9, v171
	v_fmac_f32_e32 v178, v10, v170
	v_fmac_f32_e32 v178, v11, v169
	v_fmac_f32_e32 v178, v12, v168
	v_fmac_f32_e32 v178, v13, v166
	v_fmac_f32_e32 v178, v14, v161
	v_fmac_f32_e32 v178, v15, v162
	v_fmac_f32_e32 v178, v16, v163
	v_fmac_f32_e32 v178, v17, v164
	v_fmac_f32_e32 v178, v18, v165
	v_fmac_f32_e32 v178, v19, v167
	v_fmac_f32_e32 v178, v20, v174
	v_fmac_f32_e32 v178, v21, v176
	v_fmac_f32_e32 v178, v22, v177
	v_fmac_f32_e32 v178, v23, v192
	v_fmac_f32_e32 v178, v152, v193
	v_fmac_f32_e32 v178, v154, v194
	v_fmac_f32_e32 v178, v155, v196
	v_fmac_f32_e32 v178, v156, v198
	v_fmac_f32_e32 v178, v157, v205
	v_fmac_f32_e32 v178, v158, v204
	v_fmac_f32_e32 v178, v159, v203
	ds_write_b32 v95, v178
	ds_read_u16 v178, v35 offset:51200
	s_waitcnt lgkmcnt(0)
; __device__ __forceinline__ void phase_even_mix(CArgs a, LAS unsigned char* lds, int i2, int wv, int xw  ) {
;     ...
;             for (int r = 0; r < 64; ++r) {
;                 win[r % 34] = bf2f(glu[r * 512 + c]);
;                 if (r >= 32) { float y = cb;
; #pragma unroll
;                     for (int k = 0; k < 31; ++k) y += w[k] * win[(r - 30 + k) % 34];
;                     ybuf[(r - 32) * 512 + c] = y; }
	v_lshlrev_b32_e32 v202, 16, v178
	v_fma_f32 v178, v0, v201, v160
	v_fmac_f32_e32 v178, v1, v200
	v_fmac_f32_e32 v178, v2, v199
	v_fmac_f32_e32 v178, v3, v197
	v_fmac_f32_e32 v178, v4, v195
	v_fmac_f32_e32 v178, v5, v175
	v_fmac_f32_e32 v178, v6, v173
	v_fmac_f32_e32 v178, v7, v172
	v_fmac_f32_e32 v178, v8, v171
	v_fmac_f32_e32 v178, v9, v170
	v_fmac_f32_e32 v178, v10, v169
	v_fmac_f32_e32 v178, v11, v168
	v_fmac_f32_e32 v178, v12, v166
	v_fmac_f32_e32 v178, v13, v161
	v_fmac_f32_e32 v178, v14, v162
	v_fmac_f32_e32 v178, v15, v163
	v_fmac_f32_e32 v178, v16, v164
	v_fmac_f32_e32 v178, v17, v165
	v_fmac_f32_e32 v178, v18, v167
	v_fmac_f32_e32 v178, v19, v174
	v_fmac_f32_e32 v178, v20, v176
	v_fmac_f32_e32 v178, v21, v177
	v_fmac_f32_e32 v178, v22, v192
	v_fmac_f32_e32 v178, v23, v193
	v_fmac_f32_e32 v178, v152, v194
	v_fmac_f32_e32 v178, v154, v196
	v_fmac_f32_e32 v178, v155, v198
	v_fmac_f32_e32 v178, v156, v205
	v_fmac_f32_e32 v178, v157, v204
	v_fmac_f32_e32 v178, v158, v203
	v_fmac_f32_e32 v178, v159, v202
	ds_write_b32 v96, v178
	ds_read_u16 v178, v35 offset:52224
	s_waitcnt lgkmcnt(0)
	v_lshlrev_b32_e32 v201, 16, v178
	v_fma_f32 v178, v0, v200, v160
	v_fmac_f32_e32 v178, v1, v199
	v_fmac_f32_e32 v178, v2, v197
	v_fmac_f32_e32 v178, v3, v195
	v_fmac_f32_e32 v178, v4, v175
	v_fmac_f32_e32 v178, v5, v173
	v_fmac_f32_e32 v178, v6, v172
	v_fmac_f32_e32 v178, v7, v171
	v_fmac_f32_e32 v178, v8, v170
	v_fmac_f32_e32 v178, v9, v169
	v_fmac_f32_e32 v178, v10, v168
	v_fmac_f32_e32 v178, v11, v166
	v_fmac_f32_e32 v178, v12, v161
	v_fmac_f32_e32 v178, v13, v162
	v_fmac_f32_e32 v178, v14, v163
	v_fmac_f32_e32 v178, v15, v164
	v_fmac_f32_e32 v178, v16, v165
	v_fmac_f32_e32 v178, v17, v167
	v_fmac_f32_e32 v178, v18, v174
	v_fmac_f32_e32 v178, v19, v176
	v_fmac_f32_e32 v178, v20, v177
	v_fmac_f32_e32 v178, v21, v192
	v_fmac_f32_e32 v178, v22, v193
	v_fmac_f32_e32 v178, v23, v194
	v_fmac_f32_e32 v178, v152, v196
	v_fmac_f32_e32 v178, v154, v198
	v_fmac_f32_e32 v178, v155, v205
	v_fmac_f32_e32 v178, v156, v204
	v_fmac_f32_e32 v178, v157, v203
	v_fmac_f32_e32 v178, v158, v202
	v_fmac_f32_e32 v178, v159, v201
	ds_write_b32 v97, v178
	ds_read_u16 v178, v35 offset:53248
	s_waitcnt lgkmcnt(0)
	v_lshlrev_b32_e32 v200, 16, v178
	v_fma_f32 v178, v0, v199, v160
	v_fmac_f32_e32 v178, v1, v197
	v_fmac_f32_e32 v178, v2, v195
	v_fmac_f32_e32 v178, v3, v175
	v_fmac_f32_e32 v178, v4, v173
	v_fmac_f32_e32 v178, v5, v172
	v_fmac_f32_e32 v178, v6, v171
	v_fmac_f32_e32 v178, v7, v170
	v_fmac_f32_e32 v178, v8, v169
	v_fmac_f32_e32 v178, v9, v168
	v_fmac_f32_e32 v178, v10, v166
	v_fmac_f32_e32 v178, v11, v161
	v_fmac_f32_e32 v178, v12, v162
	v_fmac_f32_e32 v178, v13, v163
	v_fmac_f32_e32 v178, v14, v164
	v_fmac_f32_e32 v178, v15, v165
	v_fmac_f32_e32 v178, v16, v167
	v_fmac_f32_e32 v178, v17, v174
	v_fmac_f32_e32 v178, v18, v176
	v_fmac_f32_e32 v178, v19, v177
	v_fmac_f32_e32 v178, v20, v192
	v_fmac_f32_e32 v178, v21, v193
	v_fmac_f32_e32 v178, v22, v194
	v_fmac_f32_e32 v178, v23, v196
	v_fmac_f32_e32 v178, v152, v198
	v_fmac_f32_e32 v178, v154, v205
	v_fmac_f32_e32 v178, v155, v204
	v_fmac_f32_e32 v178, v156, v203
	v_fmac_f32_e32 v178, v157, v202
	v_fmac_f32_e32 v178, v158, v201
	v_fmac_f32_e32 v178, v159, v200
	ds_write_b32 v98, v178
	ds_read_u16 v178, v35 offset:54272
	s_waitcnt lgkmcnt(0)
	v_lshlrev_b32_e32 v199, 16, v178
	v_fma_f32 v178, v0, v197, v160
	v_fmac_f32_e32 v178, v1, v195
	v_fmac_f32_e32 v178, v2, v175
	v_fmac_f32_e32 v178, v3, v173
	v_fmac_f32_e32 v178, v4, v172
	v_fmac_f32_e32 v178, v5, v171
	v_fmac_f32_e32 v178, v6, v170
	v_fmac_f32_e32 v178, v7, v169
	v_fmac_f32_e32 v178, v8, v168
	v_fmac_f32_e32 v178, v9, v166
	v_fmac_f32_e32 v178, v10, v161
	v_fmac_f32_e32 v178, v11, v162
	v_fmac_f32_e32 v178, v12, v163
	v_fmac_f32_e32 v178, v13, v164
	v_fmac_f32_e32 v178, v14, v165
	v_fmac_f32_e32 v178, v15, v167
	v_fmac_f32_e32 v178, v16, v174
	v_fmac_f32_e32 v178, v17, v176
	v_fmac_f32_e32 v178, v18, v177
	v_fmac_f32_e32 v178, v19, v192
	v_fmac_f32_e32 v178, v20, v193
	v_fmac_f32_e32 v178, v21, v194
	v_fmac_f32_e32 v178, v22, v196
	v_fmac_f32_e32 v178, v23, v198
	v_fmac_f32_e32 v178, v152, v205
	v_fmac_f32_e32 v178, v154, v204
	v_fmac_f32_e32 v178, v155, v203
	v_fmac_f32_e32 v178, v156, v202
	v_fmac_f32_e32 v178, v157, v201
	v_fmac_f32_e32 v178, v158, v200
	v_fmac_f32_e32 v178, v159, v199
	ds_write_b32 v99, v178
	ds_read_u16 v178, v35 offset:55296
	s_waitcnt lgkmcnt(0)
; __device__ __forceinline__ void phase_even_mix(CArgs a, LAS unsigned char* lds, int i2, int wv, int xw  ) {
;     ...
;             for (int r = 0; r < 64; ++r) {
;                 win[r % 34] = bf2f(glu[r * 512 + c]);
;                 if (r >= 32) { float y = cb;
; #pragma unroll
;                     for (int k = 0; k < 31; ++k) y += w[k] * win[(r - 30 + k) % 34];
;                     ybuf[(r - 32) * 512 + c] = y; }
	v_lshlrev_b32_e32 v197, 16, v178
	v_fma_f32 v178, v0, v195, v160
	v_fmac_f32_e32 v178, v1, v175
	v_fma_f32 v175, v0, v175, v160
	v_fmac_f32_e32 v175, v1, v173
	v_fmac_f32_e32 v175, v2, v172
	v_fmac_f32_e32 v175, v3, v171
	v_fmac_f32_e32 v175, v4, v170
	v_fmac_f32_e32 v175, v5, v169
	v_fmac_f32_e32 v175, v6, v168
	v_fmac_f32_e32 v178, v2, v173
	v_fmac_f32_e32 v175, v7, v166
	v_fma_f32 v173, v0, v173, v160
	v_fmac_f32_e32 v175, v8, v161
	v_fmac_f32_e32 v173, v1, v172
	v_fmac_f32_e32 v175, v9, v162
	v_fmac_f32_e32 v173, v2, v171
	v_fmac_f32_e32 v175, v10, v163
	v_fmac_f32_e32 v173, v3, v170
	v_fmac_f32_e32 v175, v11, v164
	v_fmac_f32_e32 v173, v4, v169
	v_fmac_f32_e32 v175, v12, v165
	v_fmac_f32_e32 v173, v5, v168
	v_fmac_f32_e32 v175, v13, v167
	v_fmac_f32_e32 v173, v6, v166
	v_fmac_f32_e32 v178, v3, v172
	v_fmac_f32_e32 v175, v14, v174
	v_fmac_f32_e32 v173, v7, v161
	v_fma_f32 v172, v0, v172, v160
	v_fmac_f32_e32 v175, v15, v176
	v_fmac_f32_e32 v173, v8, v162
	v_fmac_f32_e32 v172, v1, v171
	v_fmac_f32_e32 v175, v16, v177
	v_fmac_f32_e32 v173, v9, v163
	v_fmac_f32_e32 v172, v2, v170
	v_fmac_f32_e32 v175, v17, v192
	v_fmac_f32_e32 v173, v10, v164
	v_fmac_f32_e32 v172, v3, v169
	v_fmac_f32_e32 v175, v18, v193
	v_fmac_f32_e32 v173, v11, v165
	v_fmac_f32_e32 v172, v4, v168
	v_fmac_f32_e32 v175, v19, v194
	v_fmac_f32_e32 v173, v12, v167
	v_fmac_f32_e32 v172, v5, v166
	v_fmac_f32_e32 v175, v20, v196
	v_fmac_f32_e32 v173, v13, v174
	v_fmac_f32_e32 v172, v6, v161
	v_fmac_f32_e32 v178, v4, v171
	v_fmac_f32_e32 v175, v21, v198
	v_fmac_f32_e32 v173, v14, v176
	v_fmac_f32_e32 v172, v7, v162
	v_fma_f32 v171, v0, v171, v160
	v_fmac_f32_e32 v175, v22, v205
	v_fmac_f32_e32 v173, v15, v177
	v_fmac_f32_e32 v172, v8, v163
	v_fmac_f32_e32 v171, v1, v170
	v_fmac_f32_e32 v175, v23, v204
	v_fmac_f32_e32 v173, v16, v192
	v_fmac_f32_e32 v172, v9, v164
	v_fmac_f32_e32 v171, v2, v169
	ds_read_u16 v195, v35 offset:56320
	v_fmac_f32_e32 v175, v152, v203
	v_fmac_f32_e32 v173, v17, v193
	v_fmac_f32_e32 v172, v10, v165
	v_fmac_f32_e32 v171, v3, v168
	v_fmac_f32_e32 v175, v154, v202
	v_fmac_f32_e32 v173, v18, v194
	v_fmac_f32_e32 v172, v11, v167
	v_fmac_f32_e32 v171, v4, v166
	v_fmac_f32_e32 v175, v155, v201
	v_fmac_f32_e32 v173, v19, v196
	v_fmac_f32_e32 v172, v12, v174
	v_fmac_f32_e32 v171, v5, v161
	v_fmac_f32_e32 v175, v156, v200
	v_fmac_f32_e32 v173, v20, v198
	v_fmac_f32_e32 v172, v13, v176
	v_fmac_f32_e32 v171, v6, v162
	v_fmac_f32_e32 v178, v5, v170
	v_fmac_f32_e32 v175, v157, v199
	v_fmac_f32_e32 v173, v21, v205
	v_fmac_f32_e32 v172, v14, v177
	v_fmac_f32_e32 v171, v7, v163
	v_fma_f32 v170, v0, v170, v160
	s_waitcnt lgkmcnt(0)
	v_lshlrev_b32_e32 v195, 16, v195
	v_fmac_f32_e32 v175, v158, v197
	v_fmac_f32_e32 v173, v22, v204
	v_fmac_f32_e32 v172, v15, v192
	v_fmac_f32_e32 v171, v8, v164
	v_fmac_f32_e32 v170, v1, v169
	v_fmac_f32_e32 v175, v159, v195
	v_fmac_f32_e32 v173, v23, v203
	v_fmac_f32_e32 v172, v16, v193
	v_fmac_f32_e32 v171, v9, v165
	v_fmac_f32_e32 v170, v2, v168
	ds_write_b32 v101, v175
	ds_read_u16 v175, v35 offset:57344
	v_fmac_f32_e32 v173, v152, v202
	v_fmac_f32_e32 v172, v17, v194
	v_fmac_f32_e32 v171, v10, v167
	v_fmac_f32_e32 v170, v3, v166
	v_fmac_f32_e32 v173, v154, v201
	v_fmac_f32_e32 v172, v18, v196
	v_fmac_f32_e32 v171, v11, v174
	v_fmac_f32_e32 v170, v4, v161
	v_fmac_f32_e32 v173, v155, v200
	v_fmac_f32_e32 v172, v19, v198
	v_fmac_f32_e32 v171, v12, v176
	v_fmac_f32_e32 v170, v5, v162
	v_fmac_f32_e32 v173, v156, v199
	v_fmac_f32_e32 v172, v20, v205
	v_fmac_f32_e32 v171, v13, v177
	v_fmac_f32_e32 v170, v6, v163
	v_fmac_f32_e32 v178, v6, v169
	v_fmac_f32_e32 v173, v157, v197
	v_fmac_f32_e32 v172, v21, v204
	v_fmac_f32_e32 v171, v14, v192
	v_fmac_f32_e32 v170, v7, v164
	v_fma_f32 v169, v0, v169, v160
	s_waitcnt lgkmcnt(0)
	v_lshlrev_b32_e32 v175, 16, v175
	v_fmac_f32_e32 v173, v158, v195
	v_fmac_f32_e32 v172, v22, v203
	v_fmac_f32_e32 v171, v15, v193
	v_fmac_f32_e32 v170, v8, v165
	v_fmac_f32_e32 v169, v1, v168
	v_fmac_f32_e32 v173, v159, v175
	v_fmac_f32_e32 v172, v23, v202
	v_fmac_f32_e32 v171, v16, v194
	v_fmac_f32_e32 v170, v9, v167
	v_fmac_f32_e32 v169, v2, v166
	ds_write_b32 v102, v173
	ds_read_u16 v173, v35 offset:58368
	v_fmac_f32_e32 v172, v152, v201
	v_fmac_f32_e32 v171, v17, v196
	v_fmac_f32_e32 v170, v10, v174
	v_fmac_f32_e32 v169, v3, v161
	v_fmac_f32_e32 v172, v154, v200
	v_fmac_f32_e32 v171, v18, v198
	v_fmac_f32_e32 v170, v11, v176
	v_fmac_f32_e32 v169, v4, v162
	v_fmac_f32_e32 v172, v155, v199
	v_fmac_f32_e32 v171, v19, v205
	v_fmac_f32_e32 v170, v12, v177
	v_fmac_f32_e32 v169, v5, v163
	v_fmac_f32_e32 v172, v156, v197
	v_fmac_f32_e32 v171, v20, v204
	v_fmac_f32_e32 v170, v13, v192
	v_fmac_f32_e32 v169, v6, v164
	v_fmac_f32_e32 v178, v7, v168
	v_fmac_f32_e32 v172, v157, v195
	v_fmac_f32_e32 v171, v21, v203
	v_fmac_f32_e32 v170, v14, v193
	v_fmac_f32_e32 v169, v7, v165
	v_fma_f32 v168, v0, v168, v160
	s_waitcnt lgkmcnt(0)
	v_lshlrev_b32_e32 v173, 16, v173
	v_fmac_f32_e32 v172, v158, v175
	v_fmac_f32_e32 v171, v22, v202
	v_fmac_f32_e32 v170, v15, v194
	v_fmac_f32_e32 v169, v8, v167
	v_fmac_f32_e32 v168, v1, v166
	v_fmac_f32_e32 v172, v159, v173
	v_fmac_f32_e32 v171, v23, v201
	v_fmac_f32_e32 v170, v16, v196
	v_fmac_f32_e32 v169, v9, v174
	v_fmac_f32_e32 v168, v2, v161
	ds_write_b32 v103, v172
	ds_read_u16 v172, v35 offset:59392
	v_fmac_f32_e32 v171, v152, v200
	v_fmac_f32_e32 v170, v17, v198
	v_fmac_f32_e32 v169, v10, v176
	v_fmac_f32_e32 v168, v3, v162
	v_fmac_f32_e32 v171, v154, v199
	v_fmac_f32_e32 v170, v18, v205
	v_fmac_f32_e32 v169, v11, v177
	v_fmac_f32_e32 v168, v4, v163
	v_fmac_f32_e32 v171, v155, v197
	v_fmac_f32_e32 v170, v19, v204
	v_fmac_f32_e32 v169, v12, v192
	v_fmac_f32_e32 v168, v5, v164
	v_fmac_f32_e32 v171, v156, v195
	v_fmac_f32_e32 v170, v20, v203
	v_fmac_f32_e32 v169, v13, v193
	v_fmac_f32_e32 v168, v6, v165
	v_fmac_f32_e32 v178, v8, v166
	v_fmac_f32_e32 v171, v157, v175
	v_fmac_f32_e32 v170, v21, v202
	v_fmac_f32_e32 v169, v14, v194
	v_fmac_f32_e32 v168, v7, v167
	v_fma_f32 v166, v0, v166, v160
	s_waitcnt lgkmcnt(0)
; __device__ __forceinline__ void phase_even_mix(CArgs a, LAS unsigned char* lds, int i2, int wv, int xw  ) {
;     ...
; #pragma clang loop unroll(full)
;             for (int r = 0; r < 64; ++r) {
;                 win[r % 34] = bf2f(glu[r * 512 + c]);
;                 if (r >= 32) { float y = cb;
; #pragma unroll
;                     for (int k = 0; k < 31; ++k) y += w[k] * win[(r - 30 + k) % 34];
;                     ybuf[(r - 32) * 512 + c] = y; }
;             }
;         }
;         __syncthreads();
	v_lshlrev_b32_e32 v172, 16, v172
	v_fmac_f32_e32 v171, v158, v173
	v_fmac_f32_e32 v170, v22, v201
	v_fmac_f32_e32 v169, v15, v196
	v_fmac_f32_e32 v168, v8, v174
	v_fmac_f32_e32 v166, v1, v161
	v_fmac_f32_e32 v171, v159, v172
	v_fmac_f32_e32 v170, v23, v200
	v_fmac_f32_e32 v169, v16, v198
	v_fmac_f32_e32 v168, v9, v176
	v_fmac_f32_e32 v166, v2, v162
	ds_write_b32 v104, v171
	ds_read_u16 v171, v35 offset:60416
	v_fmac_f32_e32 v170, v152, v199
	v_fmac_f32_e32 v169, v17, v205
	v_fmac_f32_e32 v168, v10, v177
	v_fmac_f32_e32 v166, v3, v163
	v_fmac_f32_e32 v170, v154, v197
	v_fmac_f32_e32 v169, v18, v204
	v_fmac_f32_e32 v168, v11, v192
	v_fmac_f32_e32 v166, v4, v164
	v_fmac_f32_e32 v170, v155, v195
	v_fmac_f32_e32 v169, v19, v203
	v_fmac_f32_e32 v168, v12, v193
	v_fmac_f32_e32 v166, v5, v165
	v_fmac_f32_e32 v170, v156, v175
	v_fmac_f32_e32 v169, v20, v202
	v_fmac_f32_e32 v168, v13, v194
	v_fmac_f32_e32 v166, v6, v167
	v_fmac_f32_e32 v170, v157, v173
	v_fmac_f32_e32 v169, v21, v201
	v_fmac_f32_e32 v168, v14, v196
	v_fmac_f32_e32 v166, v7, v174
	v_fmac_f32_e32 v160, v0, v161
	s_waitcnt lgkmcnt(0)
	v_lshlrev_b32_e32 v171, 16, v171
	v_fmac_f32_e32 v170, v158, v172
	v_fmac_f32_e32 v169, v22, v200
	v_fmac_f32_e32 v168, v15, v198
	v_fmac_f32_e32 v166, v8, v176
	v_fmac_f32_e32 v160, v1, v162
	v_fmac_f32_e32 v170, v159, v171
	v_fmac_f32_e32 v169, v23, v199
	v_fmac_f32_e32 v168, v16, v205
	v_fmac_f32_e32 v166, v9, v177
	v_fmac_f32_e32 v160, v2, v163
	ds_write_b32 v105, v170
	ds_read_u16 v170, v35 offset:61440
	v_fmac_f32_e32 v169, v152, v197
	v_fmac_f32_e32 v168, v17, v204
	v_fmac_f32_e32 v166, v10, v192
	v_fmac_f32_e32 v160, v3, v164
	v_fmac_f32_e32 v169, v154, v195
	v_fmac_f32_e32 v168, v18, v203
	v_fmac_f32_e32 v166, v11, v193
	v_fmac_f32_e32 v160, v4, v165
	v_fmac_f32_e32 v169, v155, v175
	v_fmac_f32_e32 v168, v19, v202
	v_fmac_f32_e32 v166, v12, v194
	v_fmac_f32_e32 v160, v5, v167
	v_fmac_f32_e32 v169, v156, v173
	v_fmac_f32_e32 v168, v20, v201
	v_fmac_f32_e32 v166, v13, v196
	v_fmac_f32_e32 v160, v6, v174
	v_fmac_f32_e32 v169, v157, v172
	v_fmac_f32_e32 v168, v21, v200
	v_fmac_f32_e32 v166, v14, v198
	v_fmac_f32_e32 v160, v7, v176
	s_waitcnt lgkmcnt(0)
	v_lshlrev_b32_e32 v170, 16, v170
	v_fmac_f32_e32 v169, v158, v171
	v_fmac_f32_e32 v168, v22, v199
	v_fmac_f32_e32 v166, v15, v205
	v_fmac_f32_e32 v160, v8, v177
	v_fmac_f32_e32 v178, v9, v161
	v_fmac_f32_e32 v169, v159, v170
	v_fmac_f32_e32 v168, v23, v197
	v_fmac_f32_e32 v166, v16, v204
	v_fmac_f32_e32 v160, v9, v192
	v_fmac_f32_e32 v178, v10, v162
	ds_write_b32 v106, v169
	ds_read_u16 v169, v35 offset:62464
	v_fmac_f32_e32 v168, v152, v195
	v_fmac_f32_e32 v166, v17, v203
	v_fmac_f32_e32 v160, v10, v193
	v_fmac_f32_e32 v178, v11, v163
	v_fmac_f32_e32 v168, v154, v175
	v_fmac_f32_e32 v166, v18, v202
	v_fmac_f32_e32 v160, v11, v194
	v_fmac_f32_e32 v178, v12, v164
	v_fmac_f32_e32 v168, v155, v173
	v_fmac_f32_e32 v166, v19, v201
	v_fmac_f32_e32 v160, v12, v196
	v_fmac_f32_e32 v178, v13, v165
	v_fmac_f32_e32 v168, v156, v172
	v_fmac_f32_e32 v166, v20, v200
	v_fmac_f32_e32 v160, v13, v198
	v_fmac_f32_e32 v178, v14, v167
	v_fmac_f32_e32 v168, v157, v171
	v_fmac_f32_e32 v166, v21, v199
	v_fmac_f32_e32 v160, v14, v205
	v_fmac_f32_e32 v178, v15, v174
	s_waitcnt lgkmcnt(0)
	v_lshlrev_b32_e32 v169, 16, v169
	v_fmac_f32_e32 v168, v158, v170
	v_fmac_f32_e32 v166, v22, v197
	v_fmac_f32_e32 v160, v15, v204
	v_fmac_f32_e32 v178, v16, v176
	v_fmac_f32_e32 v168, v159, v169
	v_fmac_f32_e32 v166, v23, v195
	v_fmac_f32_e32 v160, v16, v203
	v_fmac_f32_e32 v178, v17, v177
	ds_write_b32 v107, v168
	ds_read_u16 v168, v35 offset:63488
	v_fmac_f32_e32 v166, v152, v175
	v_fmac_f32_e32 v160, v17, v202
	v_fmac_f32_e32 v178, v18, v192
	v_fmac_f32_e32 v166, v154, v173
	v_fmac_f32_e32 v160, v18, v201
	v_fmac_f32_e32 v178, v19, v193
	v_fmac_f32_e32 v166, v155, v172
	v_fmac_f32_e32 v160, v19, v200
	v_fmac_f32_e32 v178, v20, v194
	v_fmac_f32_e32 v166, v156, v171
	v_fmac_f32_e32 v160, v20, v199
	v_fmac_f32_e32 v178, v21, v196
	v_fmac_f32_e32 v166, v157, v170
	v_fmac_f32_e32 v160, v21, v197
	v_fmac_f32_e32 v178, v22, v198
	s_waitcnt lgkmcnt(0)
	v_lshlrev_b32_e32 v168, 16, v168
	v_fmac_f32_e32 v166, v158, v169
	v_fmac_f32_e32 v160, v22, v195
	v_fmac_f32_e32 v178, v23, v205
	v_fmac_f32_e32 v166, v159, v168
	v_fmac_f32_e32 v160, v23, v175
	v_fmac_f32_e32 v178, v152, v204
	ds_write_b32 v108, v166
	ds_read_u16 v166, v35 offset:64512
	v_fmac_f32_e32 v160, v152, v173
	v_fmac_f32_e32 v178, v154, v203
	v_fmac_f32_e32 v160, v154, v172
	v_fmac_f32_e32 v178, v155, v202
	v_fmac_f32_e32 v160, v155, v171
	v_fmac_f32_e32 v178, v156, v201
	v_fmac_f32_e32 v160, v156, v170
	v_fmac_f32_e32 v178, v157, v200
	v_fmac_f32_e32 v160, v157, v169
	v_fmac_f32_e32 v178, v158, v199
	s_waitcnt lgkmcnt(0)
	v_lshlrev_b32_e32 v166, 16, v166
	v_fmac_f32_e32 v160, v158, v168
	v_add_u32_e32 v152, s19, v69
	v_fmac_f32_e32 v178, v159, v197
	v_fmac_f32_e32 v160, v159, v166
	v_cmp_lt_i32_e32 vcc, -1, v152
	v_mov_b32_e32 v0, 0
	v_mov_b32_e32 v2, 0
	v_mov_b32_e32 v3, 0
	v_mov_b32_e32 v4, 0
	v_mov_b32_e32 v5, 0
	ds_write_b32 v100, v178
	ds_write_b32 v109, v160
	s_waitcnt lgkmcnt(0)
	s_barrier
; #define LAS __attribute__((address_space(3)))
; __device__ __forceinline__ void phase_even_mix(CArgs a, LAS unsigned char* lds, int i2, int wv, int xw  ) {
;     ...
;         for (int it = 0; it < 6; ++it) { const int item = it * NTHR + tid, tt = item >> 6, cg = item & 63, p = t0 - 16 + tt;
;             u32x4 o = (u32x4){0u, 0u, 0u, 0u};
;             if (p >= 0) o = *(const u32x4*)(HB + ((size_t)b * SEQ + p) * EVEN_IN + cg * 8);
;             *(LAS u32x4*)(glu + tt * 512 + cg * 8) = o; }
	v_add_u32_e32 v152, s19, v69
	v_mov_b32_e32 v200, 0
	v_cmp_lt_i32_e32 vcc, -1, v152
	v_mov_b32_e32 v201, 0
	v_mov_b32_e32 v202, 0
	v_mov_b32_e32 v203, 0
	s_nop 0
	s_and_saveexec_b64 s[16:17], vcc
	v_lshl_add_u64 v[0:1], s[92:93], 0, v[152:153]
	v_mad_u64_u32 v[2:3], s[22:23], v0, s53, v[24:25]
	v_mad_i32_i24 v3, v1, s53, v3
	global_load_dwordx4 v[200:203], v[2:3], off
	s_or_b64 exec, exec, s[16:17]
	v_add_u32_e32 v152, s19, v70
	v_mov_b32_e32 v204, 0
	v_cmp_lt_i32_e32 vcc, -1, v152
	v_mov_b32_e32 v205, 0
	v_mov_b32_e32 v206, 0
	v_mov_b32_e32 v207, 0
	s_nop 0
	s_and_saveexec_b64 s[16:17], vcc
	v_lshl_add_u64 v[0:1], s[92:93], 0, v[152:153]
	v_mad_u64_u32 v[2:3], s[22:23], v0, s53, v[24:25]
	v_mad_i32_i24 v3, v1, s53, v3
	global_load_dwordx4 v[204:207], v[2:3], off
	s_or_b64 exec, exec, s[16:17]
	v_add_u32_e32 v152, s19, v71
	v_mov_b32_e32 v208, 0
	v_cmp_lt_i32_e32 vcc, -1, v152
	v_mov_b32_e32 v209, 0
	v_mov_b32_e32 v210, 0
	v_mov_b32_e32 v211, 0
	s_nop 0
	s_and_saveexec_b64 s[16:17], vcc
	v_lshl_add_u64 v[0:1], s[92:93], 0, v[152:153]
	v_mad_u64_u32 v[2:3], s[22:23], v0, s53, v[24:25]
	v_mad_i32_i24 v3, v1, s53, v3
	global_load_dwordx4 v[208:211], v[2:3], off
	s_or_b64 exec, exec, s[16:17]
	v_add_u32_e32 v152, s19, v72
	v_mov_b32_e32 v212, 0
	v_cmp_lt_i32_e32 vcc, -1, v152
	v_mov_b32_e32 v213, 0
	v_mov_b32_e32 v214, 0
	v_mov_b32_e32 v215, 0
	s_nop 0
	s_and_saveexec_b64 s[16:17], vcc
	v_lshl_add_u64 v[0:1], s[92:93], 0, v[152:153]
	v_mad_u64_u32 v[2:3], s[22:23], v0, s53, v[24:25]
	v_mad_i32_i24 v3, v1, s53, v3
	global_load_dwordx4 v[212:215], v[2:3], off
	s_or_b64 exec, exec, s[16:17]
	v_add_u32_e32 v152, s19, v73
	v_mov_b32_e32 v216, 0
	v_cmp_lt_i32_e32 vcc, -1, v152
	v_mov_b32_e32 v217, 0
	v_mov_b32_e32 v218, 0
	v_mov_b32_e32 v219, 0
	s_nop 0
	s_and_saveexec_b64 s[16:17], vcc
	v_lshl_add_u64 v[0:1], s[92:93], 0, v[152:153]
	v_mad_u64_u32 v[2:3], s[22:23], v0, s53, v[24:25]
	v_mad_i32_i24 v3, v1, s53, v3
	global_load_dwordx4 v[216:219], v[2:3], off
	s_or_b64 exec, exec, s[16:17]
	v_add_u32_e32 v152, s19, v74
	v_mov_b32_e32 v220, 0
	v_cmp_lt_i32_e32 vcc, -1, v152
	v_mov_b32_e32 v221, 0
	v_mov_b32_e32 v222, 0
	v_mov_b32_e32 v223, 0
	s_nop 0
	s_and_saveexec_b64 s[16:17], vcc
	v_lshl_add_u64 v[0:1], s[92:93], 0, v[152:153]
	v_mad_u64_u32 v[2:3], s[22:23], v0, s53, v[24:25]
	v_mad_i32_i24 v3, v1, s53, v3
	global_load_dwordx4 v[220:223], v[2:3], off
	s_or_b64 exec, exec, s[16:17]
	s_waitcnt vmcnt(5)
	ds_write_b128 v146, v[200:203]
	s_waitcnt vmcnt(4)
	ds_write_b128 v147, v[204:207]
	s_waitcnt vmcnt(3)
	ds_write_b128 v148, v[208:211]
	s_waitcnt vmcnt(2)
	ds_write_b128 v149, v[212:215]
	s_waitcnt vmcnt(1)
	ds_write_b128 v150, v[216:219]
	s_waitcnt vmcnt(0)
	ds_write_b128 v151, v[220:223]
	s_branch .LBB0_460
